# attention key-block loops: QK^T chain waits only on LDS (hipcc's merged vmcnt drained the LDS-DMA prefetch of the block two steps ahead every iteration); + K-loop blanket lgkmcnt removal
# speedup vs baseline: 1.0027x; 1.0027x over previous
; #define LDS_AS __attribute__((address_space(3)))
; #define MFMA32(a, b, c) __builtin_amdgcn_mfma_f32_32x32x16_bf16((a), (b), (c), 0, 0, 0)
; DI void attn_mla_item(const Params& p, LDS_AS unsigned char* lds, const AttnCtx& c, int qb, int nsteps) {
;     ...
;   for (; s < nsteps; ++s) {
;     const int kb = nsteps - 1 - s;
;     if (s + 2 < nsteps) { attn_issue(c, kb - 2, rb == 0 ? 2 : rb - 1); }
;     LDS_AS unsigned char* Bf = lds + rb * AT_BUF;
;     bf16x8 kf[12];
; #pragma unroll
;     for (int ks = 0; ks < 8; ++ks) kf[ks] = *(const LDS_AS bf16x8*)(Bf + AT_MLK + offb((unsigned)l31, (unsigned)(2 * ks + hh)));
; #pragma unroll
;     for (int ks = 0; ks < 4; ++ks) kf[8 + ks] = *(const LDS_AS bf16x8*)(Bf + AT_MLR + 128u * (unsigned)l31 + 16u * ((unsigned)(2 * ks + hh) ^ ((unsigned)l31 & 7u)));
;     __builtin_amdgcn_sched_barrier(0);
;     f32x16 z;
; #pragma unroll
;     for (int i = 0; i < 16; ++i) z[i] = 0.f;
; #pragma unroll
;     for (int ks = 0; ks < 12; ++ks) z = MFMA32(kf[ks], qf[ks], z);
;     const float c2 = 0.10411754584378834f;
;     float mx = fmaxf(fmaxf(z[0], z[1]), fmaxf(z[2], z[3]));
; #pragma unroll
;     for (int i = 4; i < 16; i += 2) mx = fmaxf(mx, fmaxf(z[i], z[i + 1]));
;     { float lo, hi; xhalf(mx, lo, hi); mx = fmaxf(lo, hi) * c2; }
;     if (__builtin_amdgcn_ballot_w64(mx - mrun > 8.f) != 0ull) {
;       const float mnew = fmaxf(mrun, mx);
;       const float alpha = __builtin_amdgcn_exp2f(mrun - mnew);
;       lrun *= alpha; mrun = mnew;
; #pragma unroll
;       for (int d = 0; d < 4; ++d)
; #pragma unroll
;         for (int i = 0; i < 16; ++i) o[d][i] *= alpha;
;     }
.LBB0_1032:
	s_add_i32 s84, s38, 0
	v_add_u32_e32 v1, s84, v140
	v_add_u32_e32 v66, v1, v153
	v_add_u32_e32 v70, v1, v154
	ds_read_b128 v[66:69], v66 offset:16400
	ds_read_b128 v[170:173], v70 offset:16400
	v_add_u32_e32 v70, v1, v155
	v_add_u32_e32 v71, v1, v156
	ds_read_b128 v[174:177], v70 offset:16400
	ds_read_b128 v[178:181], v71 offset:16400
	v_add_u32_e32 v70, v1, v157
	v_add_u32_e32 v71, v1, v158
	ds_read_b128 v[182:185], v70 offset:16400
	ds_read_b128 v[186:189], v71 offset:16400
	v_add_u32_e32 v70, v1, v159
	v_add_u32_e32 v1, v1, v160
	ds_read_b128 v[192:195], v70 offset:16400
	ds_read_b128 v[196:199], v1 offset:16400
	v_add_u32_e32 v1, s84, v141
	v_add_u32_e32 v70, v1, v161
	v_add_u32_e32 v71, v1, v162
	ds_read_b128 v[200:203], v70 offset:24592
	ds_read_b128 v[204:207], v71 offset:24592
	v_add_u32_e32 v70, v1, v163
	v_add_u32_e32 v1, v1, v164
	ds_read_b128 v[208:211], v70 offset:24592
	ds_read_b128 v[212:215], v1 offset:24592
	s_waitcnt lgkmcnt(11)
	v_mfma_f32_32x32x16_bf16 v[66:81], v[66:69], v[82:85], 0
	s_mov_b32 s38, 0x41000000
	s_waitcnt lgkmcnt(10)
	v_mfma_f32_32x32x16_bf16 v[66:81], v[170:173], v[86:89], v[66:81]
	s_waitcnt lgkmcnt(9)
	v_mfma_f32_32x32x16_bf16 v[66:81], v[174:177], v[90:93], v[66:81]
	s_waitcnt lgkmcnt(8)
	v_mfma_f32_32x32x16_bf16 v[66:81], v[178:181], v[94:97], v[66:81]
	s_waitcnt lgkmcnt(7)
	v_mfma_f32_32x32x16_bf16 v[66:81], v[182:185], v[98:101], v[66:81]
	s_waitcnt lgkmcnt(6)
	v_mfma_f32_32x32x16_bf16 v[66:81], v[186:189], v[102:105], v[66:81]
	s_waitcnt lgkmcnt(5)
	v_mfma_f32_32x32x16_bf16 v[66:81], v[192:195], v[106:109], v[66:81]
	s_waitcnt lgkmcnt(4)
	v_mfma_f32_32x32x16_bf16 v[66:81], v[196:199], v[110:113], v[66:81]
	s_waitcnt lgkmcnt(3)
	v_mfma_f32_32x32x16_bf16 v[66:81], v[200:203], v[114:117], v[66:81]
	s_waitcnt lgkmcnt(2)
	v_mfma_f32_32x32x16_bf16 v[66:81], v[204:207], v[118:121], v[66:81]
	s_waitcnt lgkmcnt(1)
	v_mfma_f32_32x32x16_bf16 v[66:81], v[208:211], v[122:125], v[66:81]
	s_waitcnt lgkmcnt(0)
	v_mfma_f32_32x32x16_bf16 v[66:81], v[212:215], v[126:129], v[66:81]
	s_nop 11
	v_max_f32_e32 v1, v69, v69
	v_max_f32_e32 v135, v68, v68
	v_max_f32_e32 v170, v71, v71
	v_max_f32_e32 v171, v70, v70
	v_max_f32_e32 v172, v73, v73
	v_max_f32_e32 v173, v72, v72
	v_max_f32_e32 v1, v135, v1
	v_max_f32_e32 v174, v75, v75
	v_max_f32_e32 v175, v74, v74
	v_max_f32_e32 v176, v77, v77
	v_max_f32_e32 v177, v76, v76
	v_max_f32_e32 v135, v171, v170
	v_max_f32_e32 v170, v173, v172
	v_max3_f32 v1, v66, v67, v1
	v_max_f32_e32 v178, v79, v79
	v_max_f32_e32 v179, v78, v78
	v_max_f32_e32 v180, v81, v81
	v_max_f32_e32 v181, v80, v80
	v_max_f32_e32 v171, v175, v174
	v_max_f32_e32 v172, v177, v176
	v_max3_f32 v1, v1, v135, v170
	v_max_f32_e32 v173, v179, v178
	v_max_f32_e32 v174, v181, v180
	v_max3_f32 v1, v1, v171, v172
	v_max3_f32 v1, v1, v173, v174
	v_mov_b32_e32 v135, v1
	s_nop 1
	v_permlane32_swap_b32_e32 v1, v135
	v_max_f32_e32 v135, v135, v135
	v_max_f32_e32 v1, v1, v1
	v_max_f32_e32 v1, v1, v135
	v_fma_f32 v135, v1, s47, -v134
	v_cmp_lt_f32_e32 vcc, s38, v135
	s_cbranch_vccz .LBB0_1034
	v_mul_f32_e32 v1, 0x3dd53b94, v1
	v_max_f32_e32 v1, v1, v1
	v_max_f32_e32 v135, v134, v134
	v_max_f32_e32 v1, v135, v1
	v_sub_f32_e32 v134, v134, v1
	v_exp_f32_e32 v134, v134
	s_nop 0
	v_pk_mul_f32 v[64:65], v[64:65], v[134:135] op_sel_hi:[1,0]
	v_pk_mul_f32 v[62:63], v[62:63], v[134:135] op_sel_hi:[1,0]
	v_pk_mul_f32 v[60:61], v[60:61], v[134:135] op_sel_hi:[1,0]
	v_pk_mul_f32 v[58:59], v[58:59], v[134:135] op_sel_hi:[1,0]
	v_pk_mul_f32 v[56:57], v[56:57], v[134:135] op_sel_hi:[1,0]
	v_pk_mul_f32 v[54:55], v[54:55], v[134:135] op_sel_hi:[1,0]
	v_pk_mul_f32 v[52:53], v[52:53], v[134:135] op_sel_hi:[1,0]
	v_pk_mul_f32 v[50:51], v[50:51], v[134:135] op_sel_hi:[1,0]
	v_pk_mul_f32 v[48:49], v[48:49], v[134:135] op_sel_hi:[1,0]
	v_pk_mul_f32 v[46:47], v[46:47], v[134:135] op_sel_hi:[1,0]
	v_pk_mul_f32 v[44:45], v[44:45], v[134:135] op_sel_hi:[1,0]
	v_pk_mul_f32 v[42:43], v[42:43], v[134:135] op_sel_hi:[1,0]
	v_pk_mul_f32 v[40:41], v[40:41], v[134:135] op_sel_hi:[1,0]
	v_pk_mul_f32 v[38:39], v[38:39], v[134:135] op_sel_hi:[1,0]
	v_pk_mul_f32 v[36:37], v[36:37], v[134:135] op_sel_hi:[1,0]
	v_pk_mul_f32 v[34:35], v[34:35], v[134:135] op_sel_hi:[1,0]
	v_pk_mul_f32 v[32:33], v[32:33], v[134:135] op_sel_hi:[1,0]
	v_pk_mul_f32 v[30:31], v[30:31], v[134:135] op_sel_hi:[1,0]
	v_pk_mul_f32 v[28:29], v[28:29], v[134:135] op_sel_hi:[1,0]
	v_pk_mul_f32 v[26:27], v[26:27], v[134:135] op_sel_hi:[1,0]
	v_pk_mul_f32 v[24:25], v[24:25], v[134:135] op_sel_hi:[1,0]
	v_pk_mul_f32 v[22:23], v[22:23], v[134:135] op_sel_hi:[1,0]
	v_pk_mul_f32 v[20:21], v[20:21], v[134:135] op_sel_hi:[1,0]
	v_pk_mul_f32 v[18:19], v[18:19], v[134:135] op_sel_hi:[1,0]
	v_pk_mul_f32 v[16:17], v[16:17], v[134:135] op_sel_hi:[1,0]
	v_pk_mul_f32 v[14:15], v[14:15], v[134:135] op_sel_hi:[1,0]
	v_pk_mul_f32 v[12:13], v[12:13], v[134:135] op_sel_hi:[1,0]
	v_pk_mul_f32 v[10:11], v[10:11], v[134:135] op_sel_hi:[1,0]
	v_pk_mul_f32 v[8:9], v[8:9], v[134:135] op_sel_hi:[1,0]
	v_pk_mul_f32 v[6:7], v[6:7], v[134:135] op_sel_hi:[1,0]
	v_pk_mul_f32 v[4:5], v[4:5], v[134:135] op_sel_hi:[1,0]
	v_pk_mul_f32 v[2:3], v[2:3], v[134:135] op_sel_hi:[1,0]
	v_mul_f32_e32 v131, v131, v134
	v_mov_b32_e32 v134, v1

; DI int crow(int reg, int h) { return (reg & 3) + 8 * (reg >> 2) + 4 * h; }
; #define LDS_AS __attribute__((address_space(3)))
; #define MFMA32(a, b, c) __builtin_amdgcn_mfma_f32_32x32x16_bf16((a), (b), (c), 0, 0, 0)
; template <bool DIAG>
; DI void sb_weights(const f32x16& z, f32x16& w, float& csum, int l31, int hh) {
;     ...
; #pragma unroll
;   for (int i = 0; i < 16; ++i) {
;     const float t = z[i] * c2;
;     const float u = __builtin_amdgcn_exp2f(-fabsf(t));
;     const float spv = fmaxf(t, 0.f) + __builtin_amdgcn_logf(1.f + u);
;     ls[i] = t - spv;
;     sp[i] = (!DIAG || (crow(i, hh) < l31)) ? spv : 0.f;
; DI void attn_sb_item(const Params& p, LDS_AS unsigned char* lds, const AttnCtx& c, int qb, int nsteps) {
;     ...
;   for (; s < nsteps; ++s) {
;     const int kb = nsteps - 1 - s;
;     if (s + 2 < nsteps) { attn_issue(c, kb - 2, rb == 0 ? 2 : rb - 1); }
;     LDS_AS unsigned char* Bf = lds + rb * AT_BUF;
;     bf16x8 kf[8];
; #pragma unroll
;     for (int ks = 0; ks < 8; ++ks) kf[ks] = *(const LDS_AS bf16x8*)(Bf + AT_SBK + offb((unsigned)l31, (unsigned)(2 * ks + hh)));
;     __builtin_amdgcn_sched_barrier(0);
;     f32x16 z;
; #pragma unroll
;     for (int i = 0; i < 16; ++i) z[i] = 0.f;
; #pragma unroll
;     for (int ks = 0; ks < 8; ++ks) z = MFMA32(kf[ks], qf[ks], z);
;     f32x16 w;
;     if (kb == qb) sb_weights<true>(z, w, csum, l31, hh); else sb_weights<false>(z, w, csum, l31, hh);
.LBB0_1055:
	s_add_i32 s62, s38, 0
	v_add_u32_e32 v1, s62, v140
	v_add_u32_e32 v66, v1, v153
	v_add_u32_e32 v70, v1, v154
	ds_read_b128 v[66:69], v66 offset:16
	s_waitcnt vmcnt(26)
	ds_read_b128 v[82:85], v70 offset:16
	v_add_u32_e32 v70, v1, v155
	v_add_u32_e32 v71, v1, v156
	s_waitcnt vmcnt(25)
	ds_read_b128 v[86:89], v70 offset:16
	s_waitcnt vmcnt(24)
	ds_read_b128 v[90:93], v71 offset:16
	v_add_u32_e32 v70, v1, v157
	v_add_u32_e32 v71, v1, v158
	s_waitcnt vmcnt(23)
	ds_read_b128 v[94:97], v70 offset:16
	ds_read_b128 v[170:173], v71 offset:16
	v_add_u32_e32 v70, v1, v159
	v_add_u32_e32 v1, v1, v160
	ds_read_b128 v[174:177], v70 offset:16
	ds_read_b128 v[178:181], v1 offset:16
	s_waitcnt lgkmcnt(7)
	v_mfma_f32_32x32x16_bf16 v[66:81], v[66:69], v[98:101], 0
	s_cmp_lg_u32 s54, s46
	s_mov_b64 s[84:85], -1
	v_add_f32_e32 v1, 0, v131
	s_waitcnt lgkmcnt(6)
	v_mfma_f32_32x32x16_bf16 v[66:81], v[82:85], v[102:105], v[66:81]
	s_waitcnt lgkmcnt(5)
	v_mfma_f32_32x32x16_bf16 v[66:81], v[86:89], v[106:109], v[66:81]
	s_waitcnt lgkmcnt(4)
	v_mfma_f32_32x32x16_bf16 v[66:81], v[90:93], v[110:113], v[66:81]
	s_waitcnt lgkmcnt(3)
	v_mfma_f32_32x32x16_bf16 v[66:81], v[94:97], v[114:117], v[66:81]
	s_waitcnt lgkmcnt(2)
	v_mfma_f32_32x32x16_bf16 v[66:81], v[170:173], v[118:121], v[66:81]
	s_waitcnt lgkmcnt(1)
	v_mfma_f32_32x32x16_bf16 v[66:81], v[174:177], v[122:125], v[66:81]
	s_waitcnt lgkmcnt(0)
	v_mfma_f32_32x32x16_bf16 v[66:81], v[178:181], v[126:129], v[66:81]
	s_nop 11
	v_mul_f32_e32 v82, 0x3e0293ee, v66
	v_exp_f32_e64 v83, -|v82|
	v_max_f32_e32 v82, 0, v82
	v_mul_f32_e32 v185, 0x3e0293ee, v67
	v_mul_f32_e32 v184, 0x3e0293ee, v68
	v_add_f32_e32 v83, 1.0, v83
	v_log_f32_e32 v83, v83
	v_mul_f32_e32 v183, 0x3e0293ee, v69
	v_mul_f32_e32 v182, 0x3e0293ee, v70
	v_mul_f32_e32 v181, 0x3e0293ee, v71
	v_add_f32_e32 v134, v82, v83
	v_mul_f32_e32 v180, 0x3e0293ee, v72
	v_mul_f32_e32 v179, 0x3e0293ee, v73
	v_mul_f32_e32 v178, 0x3e0293ee, v74
	v_mul_f32_e32 v177, 0x3e0293ee, v75
	v_mul_f32_e32 v176, 0x3e0293ee, v76
	v_mul_f32_e32 v175, 0x3e0293ee, v77
	v_mul_f32_e32 v174, 0x3e0293ee, v78
	v_mul_f32_e32 v173, 0x3e0293ee, v79
	v_mul_f32_e32 v172, 0x3e0293ee, v80
	v_fma_f32 v170, v66, s48, -v134
	v_mul_f32_e32 v171, 0x3e0293ee, v81
	s_cbranch_scc0 .LBB0_1057
; DI int crow(int reg, int h) { return (reg & 3) + 8 * (reg >> 2) + 4 * h; }
; template <bool DIAG>
; DI void sb_weights(const f32x16& z, f32x16& w, float& csum, int l31, int hh) {
;   const float c2 = 0.12751743074602268f;
;   float sp[16], ls[16];
; #pragma unroll
;   for (int i = 0; i < 16; ++i) {
;     const float t = z[i] * c2;
;     const float u = __builtin_amdgcn_exp2f(-fabsf(t));
;     const float spv = fmaxf(t, 0.f) + __builtin_amdgcn_logf(1.f + u);
;     ls[i] = t - spv;
;     sp[i] = (!DIAG || (crow(i, hh) < l31)) ? spv : 0.f;
;   }
;   float R[4], Rp[4];
; #pragma unroll
;   for (int g = 0; g < 4; ++g) { R[g] = (sp[4 * g] + sp[4 * g + 1]) + (sp[4 * g + 2] + sp[4 * g + 3]); float lo, hi; xhalf(R[g], lo, hi); Rp[g] = hh ? lo : hi; }
;   float later = 0.f;
; #pragma unroll
;   for (int g = 3; g >= 0; --g) {
;     const float base = csum + later + (hh == 0 ? Rp[g] : 0.f);
;     float sfx = 0.f;
; #pragma unroll
;     for (int e = 3; e >= 0; --e) {
;       const int i = 4 * g + e;
;       const float wv = __builtin_amdgcn_exp2f(ls[i] - (base + sfx));
;       w[i] = (!DIAG || (crow(i, hh) < l31)) ? wv : 0.f;
;       sfx += sp[i];
;     }
;     later += R[g] + Rp[g];
;   }
;   csum += later;
; }
	v_exp_f32_e64 v66, -|v185|
	v_exp_f32_e64 v83, -|v184|
	v_exp_f32_e64 v85, -|v181|
	v_max_f32_e32 v96, 0, v182
	v_add_f32_e32 v66, 1.0, v66
	v_log_f32_e32 v86, v66
	v_add_f32_e32 v66, 1.0, v83
	v_log_f32_e32 v88, v66
	v_exp_f32_e64 v66, -|v182|
	v_exp_f32_e64 v83, -|v183|
	v_max_f32_e32 v97, 0, v181
	v_max_f32_e32 v190, 0, v177
	v_add_f32_e32 v66, 1.0, v66
	v_log_f32_e32 v94, v66
	v_add_f32_e32 v66, 1.0, v85
	v_add_f32_e32 v83, 1.0, v83
	v_log_f32_e32 v95, v66
	v_exp_f32_e64 v66, -|v180|
	v_log_f32_e32 v92, v83
	v_exp_f32_e64 v83, -|v179|
	v_pk_add_f32 v[186:187], v[96:97], v[94:95]
	v_add_f32_e32 v66, 1.0, v66
	v_log_f32_e32 v94, v66
	v_add_f32_e32 v66, 1.0, v83
	v_exp_f32_e64 v83, -|v178|
	v_log_f32_e32 v95, v66
	v_exp_f32_e64 v85, -|v177|
	v_max_f32_e32 v96, 0, v180
	v_max_f32_e32 v97, 0, v179
	v_add_f32_e32 v83, 1.0, v83
	v_pk_add_f32 v[188:189], v[96:97], v[94:95]
	v_log_f32_e32 v96, v83
	v_add_f32_e32 v83, 1.0, v85
	v_exp_f32_e64 v85, -|v176|
	v_log_f32_e32 v192, v83
	v_exp_f32_e64 v83, -|v175|
	v_max_f32_e32 v94, 0, v178
	v_add_f32_e32 v85, 1.0, v85
	v_log_f32_e32 v97, v85
	v_add_f32_e32 v83, 1.0, v83
	v_exp_f32_e64 v85, -|v174|
	v_log_f32_e32 v193, v83
	v_exp_f32_e64 v83, -|v173|
	v_max_f32_e32 v95, 0, v176
	v_add_f32_e32 v85, 1.0, v85
	v_log_f32_e32 v196, v85
	v_add_f32_e32 v83, 1.0, v83
	v_exp_f32_e64 v85, -|v172|
	v_log_f32_e32 v200, v83
	v_exp_f32_e64 v83, -|v171|
	v_max_f32_e32 v191, 0, v175
	v_add_f32_e32 v85, 1.0, v85
	v_log_f32_e32 v197, v85
	v_add_f32_e32 v83, 1.0, v83
	v_log_f32_e32 v201, v83
	v_pk_add_f32 v[206:207], v[94:95], v[96:97]
	v_pk_add_f32 v[190:191], v[190:191], v[192:193]
	v_max_f32_e32 v194, 0, v174
	v_max_f32_e32 v198, 0, v173
	v_max_f32_e32 v195, 0, v172
	v_max_f32_e32 v199, 0, v171
	v_pk_add_f32 v[94:95], v[206:207], v[190:191]
	v_pk_add_f32 v[202:203], v[186:187], v[186:187] op_sel_hi:[0,1]
	v_pk_add_f32 v[192:193], v[94:95], v[94:95] op_sel:[0,1] op_sel_hi:[1,0]
	v_pk_add_f32 v[94:95], v[194:195], v[196:197]
	v_pk_add_f32 v[194:195], v[198:199], v[200:201]
	v_mov_b32_e32 v83, v192
	v_mov_b32_e32 v85, v192
	v_pk_add_f32 v[96:97], v[94:95], v[194:195]
	s_nop 0
	v_permlane32_swap_b32_e32 v83, v85
	v_add_f32_e32 v93, v96, v97
	v_cndmask_b32_e64 v89, v83, v85, s[2:3]
	v_fma_f32 v83, v78, s48, -v94
	v_mov_b32_e32 v94, v93
	v_mov_b32_e32 v96, v93
	s_nop 1
	v_permlane32_swap_b32_e32 v94, v96
	v_cndmask_b32_e64 v135, v94, v96, s[2:3]
	v_cndmask_b32_e64 v97, 0, v135, s[2:3]
	v_mov_b32_e32 v196, v195
	v_mov_b32_e32 v197, v1
	v_mov_b32_e32 v96, v0
	v_fma_f32 v91, v81, s48, -v195
	v_pk_add_f32 v[196:197], v[196:197], v[96:97]
	v_fma_f32 v87, v80, s48, -v95
	v_sub_f32_e32 v91, v91, v197
	v_exp_f32_e32 v97, v91
	v_add_f32_e32 v91, v196, v197
	v_sub_f32_e32 v87, v87, v91
	v_exp_f32_e32 v96, v87
	v_add_f32_e32 v87, v95, v196
	v_fma_f32 v85, v79, s48, -v194
	v_add_f32_e32 v91, v87, v197
	v_sub_f32_e32 v85, v85, v91
	v_exp_f32_e32 v95, v85
	v_add_f32_e32 v85, v194, v87
	v_add_f32_e32 v85, v85, v197
	v_pk_add_f32 v[204:205], v[188:189], v[188:189] op_sel_hi:[0,1]
	v_sub_f32_e32 v83, v83, v85
	v_max_f32_e32 v82, 0, v185
	v_exp_f32_e32 v94, v83
	v_mov_b32_e32 v83, v203
	v_mov_b32_e32 v87, v205
	v_pk_add_f32 v[82:83], v[82:83], v[86:87]
	v_max_f32_e32 v84, 0, v184
	v_mov_b32_e32 v86, v83
	v_mov_b32_e32 v87, v83
	v_max_f32_e32 v90, 0, v183
	v_add_f32_e32 v91, v93, v135
	v_mov_b32_e32 v85, v192
	v_mov_b32_e32 v93, v0
	v_permlane32_swap_b32_e32 v86, v87
	v_pk_add_f32 v[194:195], v[84:85], v[88:89]
	v_pk_add_f32 v[84:85], v[90:91], v[92:93]
	v_cndmask_b32_e64 v135, v86, v87, s[2:3]
	v_cndmask_b32_e64 v193, 0, v89, s[2:3]
	v_pk_add_f32 v[86:87], v[194:195], v[84:85]
	v_pk_add_f32 v[88:89], v[134:135], v[82:83]
	v_mov_b32_e32 v192, v191
	v_pk_add_f32 v[196:197], v[88:89], v[86:87]
	v_add_f32_e32 v89, v131, v85
	v_mov_b32_e32 v83, v196
	v_mov_b32_e32 v86, v196
	v_mov_b32_e32 v88, v0
	v_fma_f32 v211, v77, s48, -v191
	v_permlane32_swap_b32_e32 v83, v86
	v_pk_add_f32 v[88:89], v[192:193], v[88:89]
	v_cndmask_b32_e64 v195, v83, v86, s[2:3]
	v_sub_f32_e32 v83, v211, v89
	v_fma_f32 v204, v76, s48, -v207
	v_exp_f32_e32 v93, v83
	v_add_f32_e32 v83, v88, v89
	v_sub_f32_e32 v83, v204, v83
	v_exp_f32_e32 v92, v83
	v_add_f32_e32 v83, v207, v88
	v_add_f32_e32 v85, v83, v89
	v_add_f32_e32 v83, v190, v83
	v_fma_f32 v208, v70, s48, -v186
	v_fma_f32 v186, v74, s48, -v206
	v_add_f32_e32 v83, v83, v89
	v_add_f32_e32 v87, v131, v87
	v_cndmask_b32_e64 v89, 0, v135, s[2:3]
	v_mov_b32_e32 v88, v189
	v_mov_b32_e32 v86, v0
	v_fma_f32 v210, v73, s48, -v189
	v_fma_f32 v202, v75, s48, -v190
	v_sub_f32_e32 v83, v186, v83
	v_pk_add_f32 v[190:191], v[88:89], v[86:87]
	v_exp_f32_e32 v90, v83
	v_sub_f32_e32 v83, v210, v191
	v_fma_f32 v209, v72, s48, -v188
	v_exp_f32_e32 v89, v83
	v_add_f32_e32 v83, v190, v191
	v_sub_f32_e32 v83, v209, v83
	v_sub_f32_e32 v85, v202, v85
	v_exp_f32_e32 v88, v83
	v_add_f32_e32 v83, v188, v190
	v_fma_f32 v66, v71, s48, -v187
	v_exp_f32_e32 v91, v85
	v_add_f32_e32 v85, v83, v191
	v_sub_f32_e32 v66, v66, v85
	v_exp_f32_e32 v87, v66
	v_add_f32_e32 v66, v187, v83
	v_add_f32_e32 v66, v66, v191
	v_add_f32_e32 v187, v131, v197
	v_cndmask_b32_e64 v85, 0, v195, s[2:3]
	v_mov_b32_e32 v186, v0
	v_fma_f32 v200, v69, s48, -v84
	v_sub_f32_e32 v66, v208, v66
	v_pk_add_f32 v[186:187], v[84:85], v[186:187]
	v_exp_f32_e32 v86, v66
	v_sub_f32_e32 v66, v200, v187
	v_fma_f32 v199, v68, s48, -v194
	v_exp_f32_e32 v85, v66
	v_add_f32_e32 v66, v186, v187
	v_sub_f32_e32 v66, v199, v66
	v_exp_f32_e32 v84, v66
	v_add_f32_e32 v66, v194, v186
	v_add_f32_e32 v83, v66, v187
	v_add_f32_e32 v66, v82, v66
	v_add_f32_e32 v66, v66, v187
	v_fma_f32 v198, v67, s48, -v82
	v_sub_f32_e32 v66, v170, v66
	v_sub_f32_e32 v83, v198, v83
	v_exp_f32_e32 v82, v66
	v_add_f32_e32 v66, v196, v195
	v_exp_f32_e32 v83, v83
	v_add_f32_e32 v135, v66, v197
	s_mov_b64 s[84:85], 0
